# v10: v8 + MoBA/SWA unit-start table copies de-serialized (loads batched, LDS writes at first barrier)
# speedup vs baseline: 1.0159x; 1.0159x over previous
; #define LAS __attribute__((address_space(3)))
; __device__ __forceinline__ float bf_lo(unsigned w) { return __uint_as_float(w << 16); }
; __device__ __forceinline__ float bf_hi(unsigned w) { return __uint_as_float(w & 0xffff0000u); }
; __device__ __forceinline__ void moba_unit(const MobaArgs& A, int b, int h, int qb, LAS unsigned char* lds, int wave, bool tables) {
;     ...
;     __syncthreads();
;     if (tables) {
;         for (int i = tid; i < NBLK * HD; i += 512) kms[i] = A.kmean[((size_t)(b * AH + h) * NBLK) * HD + i];
;         for (int i = tid; i < LUTA_N; i += 512) lut[i] = A.lut[h * LUTA_N + i]; }
;     stage_tile<64>(lds + L_BUF, Kh + (size_t)q0 * 512, Vh + (size_t)q0 * 512, 512, 512, wid, lane);
;     const int qpos = q0 + 32 * wid + r32;
;     bf16x8 qr[4];
;     { const bf16_t* qp = A.Q + (rowb + qpos) * 512 + h * HD + hi * 8;
; #pragma unroll
;       for (int d0 = 0; d0 < 4; ++d0) qr[d0] = *(const bf16x8*)(qp + d0 * 16); }
;     asm volatile("s_waitcnt vmcnt(0) lgkmcnt(0)" ::: "memory");
;     __syncthreads();
;     unsigned selmask = 0u;
;     if (qb > 0) {
;         float sc[NBLK];
; #pragma unroll
;         for (int n = 0; n < NBLK; ++n) { float a = 0.f;
;             if (n < qb) {
; #pragma unroll
;                 for (int d0 = 0; d0 < 4; ++d0) { const f32x4 k0 = *(const LAS f32x4*)(kms + n * HD + d0 * 16 + hi * 8), k1 = *(const LAS f32x4*)(kms + n * HD + d0 * 16 + hi * 8 + 4);
;                     const u32x4 qw = __builtin_bit_cast(u32x4, qr[d0]);
;                     a += bf_lo(qw.x) * k0[0] + bf_hi(qw.x) * k0[1] + bf_lo(qw.y) * k0[2] + bf_hi(qw.y) * k0[3] + bf_lo(qw.z) * k1[0] + bf_hi(qw.z) * k1[1] + bf_lo(qw.w) * k1[2] + bf_hi(qw.w) * k1[3]; }
;                 a += __shfl_xor(a, 32);
;             }
;             sc[n] = a; }
.LBB0_581:
	s_ashr_i32 s3, s2, 31
	s_lshr_b32 s3, s3, 29
	s_add_i32 s3, s2, s3
	s_ashr_i32 s4, s3, 3
	s_and_b32 s3, s3, -8
	s_sub_i32 s2, s2, s3
	s_mov_b32 s3, s93
	s_nop 0
	v_mbcnt_lo_u32_b32 v0, -1, s3
	v_mbcnt_hi_u32_b32 v0, -1, v0
	v_add_u32_e32 v130, s94, v0
	s_movk_i32 s3, 0x400
	s_waitcnt lgkmcnt(0)
	v_readfirstlane_b32 s30, v130
	v_cmp_gt_i32_e32 vcc, s3, v130
	s_barrier
	s_and_saveexec_b64 s[6:7], vcc
	s_mov_b64 s[10:11], 0x800
	s_cbranch_execz .LBB0_584
	s_lshl_b32 s3, s4, 3
	s_add_i32 s8, s3, s2
	s_ashr_i32 s9, s8, 31
	s_add_i32 s3, 0, 0x10000
	s_lshl_b64 s[8:9], s[8:9], 12
	v_lshl_add_u32 v210, v130, 2, s3
	v_readlane_b32 s3, v255, 40
	s_add_u32 s8, s3, s8
	v_readlane_b32 s3, v255, 42
	v_ashrrev_i32_e32 v131, 31, v130
	s_addc_u32 s9, s3, s9
	v_lshl_add_u64 v[0:1], v[130:131], 2, s[8:9]
	flat_load_dword v206, v[0:1]
	flat_load_dword v207, v[0:1] offset:2048
.LBB0_584:
	s_or_b64 exec, exec, s[6:7]
	s_movk_i32 s3, 0x540
	v_cmp_gt_i32_e32 vcc, s3, v130
	s_and_saveexec_b64 s[6:7], vcc
	s_cbranch_execz .LBB0_587
	v_readlane_b32 s3, v254, 13
	s_nop 1
	v_lshl_add_u32 v212, v130, 2, s3
	s_mul_i32 s3, s2, 0x540
	v_add_u32_e32 v2, s3, v130
	v_add_u32_e32 v2, 0x200, v2
	v_ashrrev_i32_e32 v3, 31, v2
	v_lshl_add_u64 v[2:3], v[2:3], 2, s[64:65]
	global_load_dword v208, v[2:3], off offset:-2048
	global_load_dword v209, v[2:3], off
	global_load_dword v211, v[2:3], off offset:2048
.LBB0_587:
	s_or_b64 exec, exec, s[6:7]
	s_xor_b32 s81, s89, 15
	s_ashr_i32 s5, s4, 31
	s_ashr_i32 s79, s30, 6
	s_lshl_b32 s92, s81, 8
	s_lshl_b64 s[90:91], s[4:5], 12
	s_lshl_b64 s[4:5], s[4:5], 22
	v_readlane_b32 s3, v255, 22
	s_add_u32 s6, s3, s4
	v_readlane_b32 s3, v255, 32
	s_addc_u32 s7, s3, s5
	s_lshl_b32 s2, s2, 6
	s_ashr_i32 s3, s2, 31
	s_lshl_b64 s[68:69], s[2:3], 1
	s_add_u32 s72, s6, s68
	s_addc_u32 s73, s7, s69
	v_readlane_b32 s2, v255, 33
	s_add_u32 s2, s2, s4
	v_readlane_b32 s3, v255, 34
	s_addc_u32 s3, s3, s5
	s_add_u32 s74, s2, s68
	s_addc_u32 s75, s3, s69
	s_lshl_b32 s31, s81, 18
	s_add_u32 s2, s72, s31
	v_and_b32_e32 v131, 63, v130
	s_addc_u32 s3, s73, 0
	s_add_u32 s4, s74, s31
	v_lshlrev_b32_e32 v112, 10, v131
	s_addc_u32 s5, s75, 0
	v_lshl_add_u64 v[0:1], s[2:3], 0, v[112:113]
	s_lshl_b32 s18, s79, 3
	s_lshl_b32 s2, s79, 10
	s_ashr_i32 s19, s18, 31
	s_add_i32 s82, s2, 0
	v_lshl_add_u64 v[0:1], s[18:19], 1, v[0:1]
	s_mov_b32 m0, s82
	s_lshl_b32 s2, s79, 4
	global_load_lds_dwordx4 v[0:1], off
	v_bfe_u32 v0, v130, 2, 4
	v_and_or_b32 v32, s2, 48, v0
	v_lshlrev_b32_e32 v112, 10, v32
	s_and_b32 s20, s18, 0xffffffe0
	v_lshlrev_b32_e32 v2, 3, v130
	s_lshl_b32 s2, s79, 5
	v_and_b32_e32 v155, 31, v130
	v_lshl_add_u64 v[0:1], s[4:5], 0, v[112:113]
	s_ashr_i32 s21, s20, 31
	v_and_b32_e32 v157, 24, v2
	s_add_i32 s96, s2, s92
	v_lshl_add_u64 v[0:1], s[20:21], 1, v[0:1]
	v_lshlrev_b32_e32 v112, 1, v157
	v_or_b32_e32 v134, s96, v155
	v_lshl_add_u64 v[0:1], v[0:1], 0, v[112:113]
	s_add_i32 m0, s82, 0x2000
	v_ashrrev_i32_e32 v135, 31, v134
	global_load_lds_dwordx4 v[0:1], off
	v_lshl_add_u64 v[0:1], s[90:91], 0, v[134:135]
	v_lshlrev_b64 v[0:1], 10, v[0:1]
	v_bfe_u32 v156, v130, 5, 1
	v_lshl_add_u64 v[0:1], s[0:1], 0, v[0:1]
	v_lshl_add_u64 v[0:1], v[0:1], 0, s[68:69]
	v_lshlrev_b32_e32 v132, 4, v156
	v_mov_b32_e32 v133, v113
	v_lshl_add_u64 v[0:1], v[0:1], 0, v[132:133]
	flat_load_dwordx4 v[114:117], v[0:1]
	flat_load_dwordx4 v[118:121], v[0:1] offset:32
	flat_load_dwordx4 v[122:125], v[0:1] offset:64
	flat_load_dwordx4 v[126:129], v[0:1] offset:96
	v_and_b32_e32 v0, 32, v130
	v_add_u32_e32 v0, 0, v0
	v_add_u32_e32 v34, 0x10000, v0
	s_waitcnt vmcnt(0) lgkmcnt(0)
	s_waitcnt vmcnt(0) lgkmcnt(0)
	ds_write_b32 v210, v206
	ds_write_b32 v210, v207 offset:2048
	ds_write_b32 v212, v208
	ds_write_b32 v212, v209 offset:2048
	ds_write_b32 v212, v211 offset:4096
	s_waitcnt lgkmcnt(0)
	s_barrier
	ds_read_b128 v[0:3], v34
	ds_read_b128 v[16:19], v34 offset:16
	ds_read_b128 v[20:23], v34 offset:64
	ds_read_b128 v[24:27], v34 offset:80
	s_cmp_lt_u32 s89, 7
	v_mov_b32_e32 v33, 0
	s_cselect_b64 s[6:7], -1, 0
	s_cmp_gt_u32 s89, 6
	v_and_b32_e32 v14, 0xffff0000, v114
	v_lshlrev_b32_e32 v8, 16, v114
	s_waitcnt lgkmcnt(3)
	v_mul_f32_e32 v28, v1, v14
	v_fmac_f32_e32 v28, v0, v8
	v_lshlrev_b32_e32 v12, 16, v115
	v_fmac_f32_e32 v28, v2, v12
	v_and_b32_e32 v10, 0xffff0000, v115
	v_fmac_f32_e32 v28, v3, v10
	v_lshlrev_b32_e32 v6, 16, v116
	v_and_b32_e32 v15, 0xffff0000, v118
	s_waitcnt lgkmcnt(2)
	v_fmac_f32_e32 v28, v16, v6
	v_and_b32_e32 v4, 0xffff0000, v116
	v_lshlrev_b32_e32 v9, 16, v118
	v_fmac_f32_e32 v28, v17, v4
	s_waitcnt lgkmcnt(1)
	v_mul_f32_e32 v17, v21, v15
	v_lshlrev_b32_e32 v13, 16, v119
	v_fmac_f32_e32 v17, v20, v9
	v_and_b32_e32 v11, 0xffff0000, v119
	v_fmac_f32_e32 v17, v22, v13
	v_lshlrev_b32_e32 v7, 16, v120
	v_fmac_f32_e32 v17, v23, v11
	v_and_b32_e32 v5, 0xffff0000, v120
	v_lshlrev_b32_e32 v2, 16, v117
	s_waitcnt lgkmcnt(0)
	v_fmac_f32_e32 v17, v24, v7
	v_lshlrev_b32_e32 v3, 16, v121
	v_fmac_f32_e32 v28, v18, v2
	v_and_b32_e32 v0, 0xffff0000, v117
	v_fmac_f32_e32 v17, v25, v5
	v_and_b32_e32 v1, 0xffff0000, v121
	v_fmac_f32_e32 v28, v19, v0
	v_fmac_f32_e32 v17, v26, v3
	ds_read_b128 v[22:25], v34 offset:128
	ds_read_b128 v[36:39], v34 offset:144
	ds_read_b128 v[40:43], v34 offset:192
	ds_read_b128 v[44:47], v34 offset:208
	v_add_f32_e32 v16, 0, v28
	v_fmac_f32_e32 v17, v27, v1
	v_and_b32_e32 v18, 0xffff0000, v122
	v_add_f32_e32 v35, v16, v17
	v_lshlrev_b32_e32 v16, 16, v122
	s_waitcnt lgkmcnt(3)
	v_mul_f32_e32 v48, v23, v18
	v_fmac_f32_e32 v48, v22, v16
	v_lshlrev_b32_e32 v20, 16, v123
	v_fmac_f32_e32 v48, v24, v20
	v_and_b32_e32 v22, 0xffff0000, v123
	v_and_b32_e32 v19, 0xffff0000, v126
	v_fmac_f32_e32 v48, v25, v22
	v_lshlrev_b32_e32 v24, 16, v124
	v_lshlrev_b32_e32 v17, 16, v126
	s_waitcnt lgkmcnt(2)
; #define LAS __attribute__((address_space(3)))
; __device__ __forceinline__ float bf_lo(unsigned w) { return __uint_as_float(w << 16); }
; __device__ __forceinline__ float bf_hi(unsigned w) { return __uint_as_float(w & 0xffff0000u); }
; __device__ __forceinline__ void moba_unit(const MobaArgs& A, int b, int h, int qb, LAS unsigned char* lds, int wave, bool tables) {
;     ...
;         for (int n = 0; n < NBLK; ++n) { float a = 0.f;
;             if (n < qb) {
; #pragma unroll
;                 for (int d0 = 0; d0 < 4; ++d0) { const f32x4 k0 = *(const LAS f32x4*)(kms + n * HD + d0 * 16 + hi * 8), k1 = *(const LAS f32x4*)(kms + n * HD + d0 * 16 + hi * 8 + 4);
;                     const u32x4 qw = __builtin_bit_cast(u32x4, qr[d0]);
;                     a += bf_lo(qw.x) * k0[0] + bf_hi(qw.x) * k0[1] + bf_lo(qw.y) * k0[2] + bf_hi(qw.y) * k0[3] + bf_lo(qw.z) * k1[0] + bf_hi(qw.z) * k1[1] + bf_lo(qw.w) * k1[2] + bf_hi(qw.w) * k1[3]; }
;                 a += __shfl_xor(a, 32);
;             }
;             sc[n] = a; }
	v_fmac_f32_e32 v48, v36, v24
	s_waitcnt lgkmcnt(1)
	v_mul_f32_e32 v36, v41, v19
	v_lshlrev_b32_e32 v21, 16, v127
	v_fmac_f32_e32 v36, v40, v17
	v_and_b32_e32 v23, 0xffff0000, v127
	v_and_b32_e32 v26, 0xffff0000, v124
	v_fmac_f32_e32 v36, v42, v21
	v_lshlrev_b32_e32 v25, 16, v128
	v_fmac_f32_e32 v48, v37, v26
	v_lshlrev_b32_e32 v28, 16, v125
	v_fmac_f32_e32 v36, v43, v23
	v_and_b32_e32 v27, 0xffff0000, v128
	v_fmac_f32_e32 v48, v38, v28
	v_and_b32_e32 v30, 0xffff0000, v125
	s_waitcnt lgkmcnt(0)
	v_fmac_f32_e32 v36, v44, v25
	v_lshlrev_b32_e32 v29, 16, v129
	v_fmac_f32_e32 v48, v39, v30
	v_fmac_f32_e32 v36, v45, v27
	ds_read_b128 v[38:41], v34 offset:256
	ds_read_b128 v[42:45], v34 offset:272
	v_and_b32_e32 v31, 0xffff0000, v129
	v_fmac_f32_e32 v36, v46, v29
	v_add_f32_e32 v35, v35, v48
	v_fmac_f32_e32 v36, v47, v31
	v_and_b32_e32 v37, 64, v251
	v_add_f32_e32 v35, v35, v36
	v_xor_b32_e32 v36, 32, v251
	v_add_u32_e32 v37, 64, v37
	v_cmp_lt_i32_e32 vcc, v36, v37
	s_waitcnt lgkmcnt(1)
	v_mul_f32_e32 v37, v39, v14
	v_fmac_f32_e32 v37, v38, v8
	v_fmac_f32_e32 v37, v40, v12
	v_fmac_f32_e32 v37, v41, v10
	s_waitcnt lgkmcnt(0)
	v_fmac_f32_e32 v37, v42, v6
	v_fmac_f32_e32 v37, v43, v4
	v_fmac_f32_e32 v37, v44, v2
	v_fmac_f32_e32 v37, v45, v0
	ds_read_b128 v[38:41], v34 offset:320
	ds_read_b128 v[42:45], v34 offset:336
	v_add_f32_e32 v37, 0, v37
	v_cndmask_b32_e32 v36, v251, v36, vcc
	v_lshlrev_b32_e32 v154, 2, v36
	s_waitcnt lgkmcnt(1)
	v_mul_f32_e32 v39, v39, v15
	v_fmac_f32_e32 v39, v38, v9
	v_fmac_f32_e32 v39, v40, v13
	v_fmac_f32_e32 v39, v41, v11
	s_waitcnt lgkmcnt(0)
	v_fmac_f32_e32 v39, v42, v7
	v_fmac_f32_e32 v39, v43, v5
	v_fmac_f32_e32 v39, v44, v3
	v_fmac_f32_e32 v39, v45, v1
	v_add_f32_e32 v37, v37, v39
	ds_read_b128 v[38:41], v34 offset:384
	ds_read_b128 v[42:45], v34 offset:400
	ds_bpermute_b32 v36, v154, v35
	s_waitcnt lgkmcnt(2)
	v_mul_f32_e32 v39, v39, v18
	v_fmac_f32_e32 v39, v38, v16
	v_fmac_f32_e32 v39, v40, v20
	v_fmac_f32_e32 v39, v41, v22
	s_waitcnt lgkmcnt(1)
	v_fmac_f32_e32 v39, v42, v24
	v_fmac_f32_e32 v39, v43, v26
	v_fmac_f32_e32 v39, v44, v28
	v_fmac_f32_e32 v39, v45, v30
	v_add_f32_e32 v37, v37, v39
	ds_read_b128 v[38:41], v34 offset:448
	ds_read_b128 v[42:45], v34 offset:464
	s_waitcnt lgkmcnt(1)
	v_mul_f32_e32 v39, v39, v19
	v_fmac_f32_e32 v39, v38, v17
	v_fmac_f32_e32 v39, v40, v21
	v_fmac_f32_e32 v39, v41, v23
	s_waitcnt lgkmcnt(0)
	v_fmac_f32_e32 v39, v42, v25
	v_fmac_f32_e32 v39, v43, v27
	v_fmac_f32_e32 v39, v44, v29
	v_fmac_f32_e32 v39, v45, v31
	ds_read_b128 v[40:43], v34 offset:512
	ds_read_b128 v[44:47], v34 offset:528
	v_add_f32_e32 v37, v37, v39
	ds_bpermute_b32 v38, v154, v37
	s_waitcnt lgkmcnt(2)
	v_mul_f32_e32 v39, v41, v14
	v_fmac_f32_e32 v39, v40, v8
	v_fmac_f32_e32 v39, v42, v12
	v_fmac_f32_e32 v39, v43, v10
	s_waitcnt lgkmcnt(1)
	v_fmac_f32_e32 v39, v44, v6
	v_fmac_f32_e32 v39, v45, v4
	v_fmac_f32_e32 v39, v46, v2
	v_fmac_f32_e32 v39, v47, v0
	ds_read_b128 v[40:43], v34 offset:576
	ds_read_b128 v[44:47], v34 offset:592
	v_add_f32_e32 v39, 0, v39
	s_waitcnt lgkmcnt(1)
	v_mul_f32_e32 v41, v41, v15
	v_fmac_f32_e32 v41, v40, v9
	v_fmac_f32_e32 v41, v42, v13
	v_fmac_f32_e32 v41, v43, v11
	s_waitcnt lgkmcnt(0)
	v_fmac_f32_e32 v41, v44, v7
	v_fmac_f32_e32 v41, v45, v5
	v_fmac_f32_e32 v41, v46, v3
	v_fmac_f32_e32 v41, v47, v1
	v_add_f32_e32 v39, v39, v41
	ds_read_b128 v[40:43], v34 offset:640
	ds_read_b128 v[44:47], v34 offset:656
	s_waitcnt lgkmcnt(1)
	v_mul_f32_e32 v41, v41, v18
	v_fmac_f32_e32 v41, v40, v16
	v_fmac_f32_e32 v41, v42, v20
	v_fmac_f32_e32 v41, v43, v22
	s_waitcnt lgkmcnt(0)
	v_fmac_f32_e32 v41, v44, v24
	v_fmac_f32_e32 v41, v45, v26
	v_fmac_f32_e32 v41, v46, v28
	v_fmac_f32_e32 v41, v47, v30
	v_add_f32_e32 v39, v39, v41
	ds_read_b128 v[40:43], v34 offset:704
	ds_read_b128 v[44:47], v34 offset:720
	s_waitcnt lgkmcnt(1)
	v_mul_f32_e32 v41, v41, v19
	v_fmac_f32_e32 v41, v40, v17
	v_fmac_f32_e32 v41, v42, v21
	v_fmac_f32_e32 v41, v43, v23
	s_waitcnt lgkmcnt(0)
	v_fmac_f32_e32 v41, v44, v25
	v_fmac_f32_e32 v41, v45, v27
	v_fmac_f32_e32 v41, v46, v29
	v_fmac_f32_e32 v41, v47, v31
	ds_read_b128 v[42:45], v34 offset:768
	ds_read_b128 v[46:49], v34 offset:784
	v_add_f32_e32 v39, v39, v41
	ds_bpermute_b32 v40, v154, v39
	s_waitcnt lgkmcnt(2)
	v_mul_f32_e32 v41, v43, v14
	v_fmac_f32_e32 v41, v42, v8
	v_fmac_f32_e32 v41, v44, v12
	v_fmac_f32_e32 v41, v45, v10
	s_waitcnt lgkmcnt(1)
	v_fmac_f32_e32 v41, v46, v6
	v_fmac_f32_e32 v41, v47, v4
	v_fmac_f32_e32 v41, v48, v2
	v_fmac_f32_e32 v41, v49, v0
	ds_read_b128 v[42:45], v34 offset:832
	ds_read_b128 v[46:49], v34 offset:848
	v_add_f32_e32 v41, 0, v41
	s_waitcnt lgkmcnt(1)
	v_mul_f32_e32 v43, v43, v15
	v_fmac_f32_e32 v43, v42, v9
	v_fmac_f32_e32 v43, v44, v13
	v_fmac_f32_e32 v43, v45, v11
	s_waitcnt lgkmcnt(0)
	v_fmac_f32_e32 v43, v46, v7
	v_fmac_f32_e32 v43, v47, v5
	v_fmac_f32_e32 v43, v48, v3
	v_fmac_f32_e32 v43, v49, v1
	v_add_f32_e32 v41, v41, v43
	ds_read_b128 v[42:45], v34 offset:896
	ds_read_b128 v[46:49], v34 offset:912
	s_waitcnt lgkmcnt(1)
	v_mul_f32_e32 v43, v43, v18
	v_fmac_f32_e32 v43, v42, v16
	v_fmac_f32_e32 v43, v44, v20
	v_fmac_f32_e32 v43, v45, v22
	s_waitcnt lgkmcnt(0)
	v_fmac_f32_e32 v43, v46, v24
	v_fmac_f32_e32 v43, v47, v26
	v_fmac_f32_e32 v43, v48, v28
	v_fmac_f32_e32 v43, v49, v30
	v_add_f32_e32 v41, v41, v43
	ds_read_b128 v[42:45], v34 offset:960
	ds_read_b128 v[46:49], v34 offset:976
	s_waitcnt lgkmcnt(1)
	v_mul_f32_e32 v43, v43, v19
	v_fmac_f32_e32 v43, v42, v17
	v_fmac_f32_e32 v43, v44, v21
	v_fmac_f32_e32 v43, v45, v23
	s_waitcnt lgkmcnt(0)
; #define LAS __attribute__((address_space(3)))
; __device__ __forceinline__ float bf_lo(unsigned w) { return __uint_as_float(w << 16); }
; __device__ __forceinline__ float bf_hi(unsigned w) { return __uint_as_float(w & 0xffff0000u); }
; __device__ __forceinline__ void moba_unit(const MobaArgs& A, int b, int h, int qb, LAS unsigned char* lds, int wave, bool tables) {
;     ...
;         for (int n = 0; n < NBLK; ++n) { float a = 0.f;
;             if (n < qb) {
; #pragma unroll
;                 for (int d0 = 0; d0 < 4; ++d0) { const f32x4 k0 = *(const LAS f32x4*)(kms + n * HD + d0 * 16 + hi * 8), k1 = *(const LAS f32x4*)(kms + n * HD + d0 * 16 + hi * 8 + 4);
;                     const u32x4 qw = __builtin_bit_cast(u32x4, qr[d0]);
;                     a += bf_lo(qw.x) * k0[0] + bf_hi(qw.x) * k0[1] + bf_lo(qw.y) * k0[2] + bf_hi(qw.y) * k0[3] + bf_lo(qw.z) * k1[0] + bf_hi(qw.z) * k1[1] + bf_lo(qw.w) * k1[2] + bf_hi(qw.w) * k1[3]; }
;                 a += __shfl_xor(a, 32);
;             }
;             sc[n] = a; }
	v_fmac_f32_e32 v43, v46, v25
	v_fmac_f32_e32 v43, v47, v27
	v_fmac_f32_e32 v43, v48, v29
	v_fmac_f32_e32 v43, v49, v31
	ds_read_b128 v[44:47], v34 offset:1024
	ds_read_b128 v[48:51], v34 offset:1040
	v_add_f32_e32 v41, v41, v43
	ds_bpermute_b32 v42, v154, v41
	s_waitcnt lgkmcnt(2)
	v_mul_f32_e32 v43, v45, v14
	v_fmac_f32_e32 v43, v44, v8
	v_fmac_f32_e32 v43, v46, v12
	v_fmac_f32_e32 v43, v47, v10
	s_waitcnt lgkmcnt(1)
	v_fmac_f32_e32 v43, v48, v6
	v_fmac_f32_e32 v43, v49, v4
	v_fmac_f32_e32 v43, v50, v2
	v_fmac_f32_e32 v43, v51, v0
	ds_read_b128 v[44:47], v34 offset:1088
	ds_read_b128 v[48:51], v34 offset:1104
	v_add_f32_e32 v43, 0, v43
	s_waitcnt lgkmcnt(1)
	v_mul_f32_e32 v45, v45, v15
	v_fmac_f32_e32 v45, v44, v9
	v_fmac_f32_e32 v45, v46, v13
	v_fmac_f32_e32 v45, v47, v11
	s_waitcnt lgkmcnt(0)
	v_fmac_f32_e32 v45, v48, v7
	v_fmac_f32_e32 v45, v49, v5
	v_fmac_f32_e32 v45, v50, v3
	v_fmac_f32_e32 v45, v51, v1
	v_add_f32_e32 v43, v43, v45
	ds_read_b128 v[44:47], v34 offset:1152
	ds_read_b128 v[48:51], v34 offset:1168
	s_waitcnt lgkmcnt(1)
	v_mul_f32_e32 v45, v45, v18
	v_fmac_f32_e32 v45, v44, v16
	v_fmac_f32_e32 v45, v46, v20
	v_fmac_f32_e32 v45, v47, v22
	s_waitcnt lgkmcnt(0)
	v_fmac_f32_e32 v45, v48, v24
	v_fmac_f32_e32 v45, v49, v26
	v_fmac_f32_e32 v45, v50, v28
	v_fmac_f32_e32 v45, v51, v30
	v_add_f32_e32 v43, v43, v45
	ds_read_b128 v[44:47], v34 offset:1216
	ds_read_b128 v[48:51], v34 offset:1232
	s_waitcnt lgkmcnt(1)
	v_mul_f32_e32 v45, v45, v19
	v_fmac_f32_e32 v45, v44, v17
	v_fmac_f32_e32 v45, v46, v21
	v_fmac_f32_e32 v45, v47, v23
	s_waitcnt lgkmcnt(0)
	v_fmac_f32_e32 v45, v48, v25
	v_fmac_f32_e32 v45, v49, v27
	v_fmac_f32_e32 v45, v50, v29
	v_fmac_f32_e32 v45, v51, v31
	ds_read_b128 v[46:49], v34 offset:1280
	ds_read_b128 v[50:53], v34 offset:1296
	v_add_f32_e32 v43, v43, v45
	ds_bpermute_b32 v44, v154, v43
	s_waitcnt lgkmcnt(2)
	v_mul_f32_e32 v45, v47, v14
	v_fmac_f32_e32 v45, v46, v8
	v_fmac_f32_e32 v45, v48, v12
	v_fmac_f32_e32 v45, v49, v10
	s_waitcnt lgkmcnt(1)
	v_fmac_f32_e32 v45, v50, v6
	v_fmac_f32_e32 v45, v51, v4
	v_fmac_f32_e32 v45, v52, v2
	v_fmac_f32_e32 v45, v53, v0
	ds_read_b128 v[46:49], v34 offset:1344
	ds_read_b128 v[50:53], v34 offset:1360
	v_add_f32_e32 v45, 0, v45
	s_waitcnt lgkmcnt(1)
	v_mul_f32_e32 v47, v47, v15
	v_fmac_f32_e32 v47, v46, v9
	v_fmac_f32_e32 v47, v48, v13
	v_fmac_f32_e32 v47, v49, v11
	s_waitcnt lgkmcnt(0)
	v_fmac_f32_e32 v47, v50, v7
	v_fmac_f32_e32 v47, v51, v5
	v_fmac_f32_e32 v47, v52, v3
	v_fmac_f32_e32 v47, v53, v1
	v_add_f32_e32 v45, v45, v47
	ds_read_b128 v[46:49], v34 offset:1408
	ds_read_b128 v[50:53], v34 offset:1424
	s_waitcnt lgkmcnt(1)
	v_mul_f32_e32 v47, v47, v18
	v_fmac_f32_e32 v47, v46, v16
	v_fmac_f32_e32 v47, v48, v20
	v_fmac_f32_e32 v47, v49, v22
	s_waitcnt lgkmcnt(0)
	v_fmac_f32_e32 v47, v50, v24
	v_fmac_f32_e32 v47, v51, v26
	v_fmac_f32_e32 v47, v52, v28
	v_fmac_f32_e32 v47, v53, v30
	v_add_f32_e32 v45, v45, v47
	ds_read_b128 v[46:49], v34 offset:1472
	ds_read_b128 v[50:53], v34 offset:1488
	s_waitcnt lgkmcnt(1)
	v_mul_f32_e32 v47, v47, v19
	v_fmac_f32_e32 v47, v46, v17
	v_fmac_f32_e32 v47, v48, v21
	v_fmac_f32_e32 v47, v49, v23
	s_waitcnt lgkmcnt(0)
	v_fmac_f32_e32 v47, v50, v25
	v_fmac_f32_e32 v47, v51, v27
	v_fmac_f32_e32 v47, v52, v29
	v_fmac_f32_e32 v47, v53, v31
	ds_read_b128 v[48:51], v34 offset:1536
	ds_read_b128 v[52:55], v34 offset:1552
	v_add_f32_e32 v45, v45, v47
	ds_bpermute_b32 v46, v154, v45
	s_waitcnt lgkmcnt(2)
	v_mul_f32_e32 v47, v49, v14
	v_fmac_f32_e32 v47, v48, v8
	v_fmac_f32_e32 v47, v50, v12
	v_fmac_f32_e32 v47, v51, v10
	s_waitcnt lgkmcnt(1)
	v_fmac_f32_e32 v47, v52, v6
	v_fmac_f32_e32 v47, v53, v4
	v_fmac_f32_e32 v47, v54, v2
	v_fmac_f32_e32 v47, v55, v0
	ds_read_b128 v[48:51], v34 offset:1600
	ds_read_b128 v[52:55], v34 offset:1616
	v_add_f32_e32 v47, 0, v47
	s_waitcnt lgkmcnt(1)
	v_mul_f32_e32 v49, v49, v15
	v_fmac_f32_e32 v49, v48, v9
	v_fmac_f32_e32 v49, v50, v13
	v_fmac_f32_e32 v49, v51, v11
	s_waitcnt lgkmcnt(0)
	v_fmac_f32_e32 v49, v52, v7
	v_fmac_f32_e32 v49, v53, v5
	v_fmac_f32_e32 v49, v54, v3
	v_fmac_f32_e32 v49, v55, v1
	v_add_f32_e32 v47, v47, v49
	ds_read_b128 v[48:51], v34 offset:1664
	ds_read_b128 v[52:55], v34 offset:1680
	s_waitcnt lgkmcnt(1)
	v_mul_f32_e32 v49, v49, v18
	v_fmac_f32_e32 v49, v48, v16
	v_fmac_f32_e32 v49, v50, v20
	v_fmac_f32_e32 v49, v51, v22
	s_waitcnt lgkmcnt(0)
	v_fmac_f32_e32 v49, v52, v24
	v_fmac_f32_e32 v49, v53, v26
	v_fmac_f32_e32 v49, v54, v28
	v_fmac_f32_e32 v49, v55, v30
	v_add_f32_e32 v47, v47, v49
	ds_read_b128 v[48:51], v34 offset:1728
	ds_read_b128 v[52:55], v34 offset:1744
	s_waitcnt lgkmcnt(1)
	v_mul_f32_e32 v49, v49, v19
	v_fmac_f32_e32 v49, v48, v17
	v_fmac_f32_e32 v49, v50, v21
	v_fmac_f32_e32 v49, v51, v23
	s_waitcnt lgkmcnt(0)
	v_fmac_f32_e32 v49, v52, v25
	v_fmac_f32_e32 v49, v53, v27
	v_fmac_f32_e32 v49, v54, v29
	v_fmac_f32_e32 v49, v55, v31
	ds_read_b128 v[54:57], v34 offset:1792
	ds_read_b128 v[58:61], v34 offset:1808
	v_add_f32_e32 v51, v47, v49
	ds_bpermute_b32 v52, v154, v51
	s_waitcnt lgkmcnt(2)
	v_mul_f32_e32 v47, v55, v14
	v_fmac_f32_e32 v47, v54, v8
	v_fmac_f32_e32 v47, v56, v12
	v_fmac_f32_e32 v47, v57, v10
	s_waitcnt lgkmcnt(1)
	v_fmac_f32_e32 v47, v58, v6
	v_fmac_f32_e32 v47, v59, v4
	v_fmac_f32_e32 v47, v60, v2
	v_fmac_f32_e32 v47, v61, v0
	ds_read_b128 v[54:57], v34 offset:1856
	ds_read_b128 v[58:61], v34 offset:1872
	v_add_f32_e32 v47, 0, v47
	s_waitcnt lgkmcnt(1)
	v_mul_f32_e32 v48, v55, v15
	v_fmac_f32_e32 v48, v54, v9
	v_fmac_f32_e32 v48, v56, v13
	v_fmac_f32_e32 v48, v57, v11
	s_waitcnt lgkmcnt(0)
	v_fmac_f32_e32 v48, v58, v7
	v_fmac_f32_e32 v48, v59, v5
	v_fmac_f32_e32 v48, v60, v3
	v_fmac_f32_e32 v48, v61, v1
	ds_read_b128 v[54:57], v34 offset:1920
	ds_read_b128 v[58:61], v34 offset:1936
	v_add_f32_e32 v47, v47, v48
	s_waitcnt lgkmcnt(1)
	v_mul_f32_e32 v48, v55, v18
	v_fmac_f32_e32 v48, v54, v16
	v_fmac_f32_e32 v48, v56, v20
	v_fmac_f32_e32 v48, v57, v22
	s_waitcnt lgkmcnt(0)
	v_fmac_f32_e32 v48, v58, v24
	v_fmac_f32_e32 v48, v59, v26
	v_fmac_f32_e32 v48, v60, v28
	v_fmac_f32_e32 v48, v61, v30
	ds_read_b128 v[54:57], v34 offset:1984
	ds_read_b128 v[58:61], v34 offset:2000
	v_add_f32_e32 v47, v47, v48
	s_waitcnt lgkmcnt(1)
	v_mul_f32_e32 v48, v55, v19
	v_fmac_f32_e32 v48, v54, v17
	v_fmac_f32_e32 v48, v56, v21
	v_fmac_f32_e32 v48, v57, v23
	s_waitcnt lgkmcnt(0)
	v_fmac_f32_e32 v48, v58, v25
	v_fmac_f32_e32 v48, v59, v27
	v_fmac_f32_e32 v48, v60, v29
	v_fmac_f32_e32 v48, v61, v31
	v_add_f32_e32 v55, v47, v48
	ds_bpermute_b32 v56, v154, v55
	v_mov_b32_e32 v47, 0
	s_cbranch_scc1 .LBB0_589
; #define LAS __attribute__((address_space(3)))
; __device__ __forceinline__ float bf_lo(unsigned w) { return __uint_as_float(w << 16); }
; __device__ __forceinline__ float bf_hi(unsigned w) { return __uint_as_float(w & 0xffff0000u); }
; __device__ __forceinline__ void moba_unit(const MobaArgs& A, int b, int h, int qb, LAS unsigned char* lds, int wave, bool tables) {
;     ...
;         for (int n = 0; n < NBLK; ++n) { float a = 0.f;
;             if (n < qb) {
; #pragma unroll
;                 for (int d0 = 0; d0 < 4; ++d0) { const f32x4 k0 = *(const LAS f32x4*)(kms + n * HD + d0 * 16 + hi * 8), k1 = *(const LAS f32x4*)(kms + n * HD + d0 * 16 + hi * 8 + 4);
;                     const u32x4 qw = __builtin_bit_cast(u32x4, qr[d0]);
;                     a += bf_lo(qw.x) * k0[0] + bf_hi(qw.x) * k0[1] + bf_lo(qw.y) * k0[2] + bf_hi(qw.y) * k0[3] + bf_lo(qw.z) * k1[0] + bf_hi(qw.z) * k1[1] + bf_lo(qw.w) * k1[2] + bf_hi(qw.w) * k1[3]; }
;                 a += __shfl_xor(a, 32);
;             }
;             sc[n] = a; }
	ds_read_b128 v[58:61], v34 offset:2048
	ds_read_b128 v[62:65], v34 offset:2112
	ds_read_b128 v[66:69], v34 offset:2064
	ds_read_b128 v[70:73], v34 offset:2128
	s_waitcnt lgkmcnt(3)
	v_mov_b32_e32 v48, v58
	s_waitcnt lgkmcnt(2)
	v_mov_b32_e32 v49, v62
	v_mov_b32_e32 v62, v59
	v_pk_mul_f32 v[58:59], v[62:63], v[14:15]
	s_nop 0
	v_pk_fma_f32 v[48:49], v[48:49], v[8:9], v[58:59]
	v_mov_b32_e32 v58, v60
	v_mov_b32_e32 v59, v64
	v_pk_fma_f32 v[48:49], v[58:59], v[12:13], v[48:49]
	v_mov_b32_e32 v64, v61
	v_pk_fma_f32 v[48:49], v[64:65], v[10:11], v[48:49]
	s_waitcnt lgkmcnt(1)
	v_mov_b32_e32 v58, v66
	s_waitcnt lgkmcnt(0)
	v_mov_b32_e32 v59, v70
	v_pk_fma_f32 v[48:49], v[58:59], v[6:7], v[48:49]
	v_mov_b32_e32 v70, v67
	v_pk_fma_f32 v[48:49], v[70:71], v[4:5], v[48:49]
	v_mov_b32_e32 v58, v68
	v_mov_b32_e32 v59, v72
	v_pk_fma_f32 v[48:49], v[58:59], v[2:3], v[48:49]
	ds_read_b128 v[58:61], v34 offset:2176
	ds_read_b128 v[62:65], v34 offset:2240
	v_mov_b32_e32 v72, v69
	v_pk_fma_f32 v[48:49], v[72:73], v[0:1], v[48:49]
	ds_read_b128 v[66:69], v34 offset:2192
	ds_read_b128 v[70:73], v34 offset:2256
	v_add_f32_e32 v47, 0, v48
	v_add_f32_e32 v47, v47, v49
	s_waitcnt lgkmcnt(2)
	v_mov_b32_e32 v49, v62
	v_mov_b32_e32 v62, v59
	v_mov_b32_e32 v48, v58
	v_pk_mul_f32 v[58:59], v[62:63], v[18:19]
	s_nop 0
	v_pk_fma_f32 v[48:49], v[48:49], v[16:17], v[58:59]
	v_mov_b32_e32 v58, v60
	v_mov_b32_e32 v59, v64
	v_pk_fma_f32 v[48:49], v[58:59], v[20:21], v[48:49]
	v_mov_b32_e32 v64, v61
	v_pk_fma_f32 v[48:49], v[64:65], v[22:23], v[48:49]
	s_waitcnt lgkmcnt(1)
	v_mov_b32_e32 v58, v66
	s_waitcnt lgkmcnt(0)
	v_mov_b32_e32 v59, v70
	v_pk_fma_f32 v[48:49], v[58:59], v[24:25], v[48:49]
	v_mov_b32_e32 v70, v67
	v_pk_fma_f32 v[48:49], v[70:71], v[26:27], v[48:49]
	v_mov_b32_e32 v58, v68
	v_mov_b32_e32 v59, v72
	v_pk_fma_f32 v[48:49], v[58:59], v[28:29], v[48:49]
	v_mov_b32_e32 v72, v69
	v_pk_fma_f32 v[48:49], v[72:73], v[30:31], v[48:49]
	s_nop 0
	v_add_f32_e32 v47, v47, v48
	v_add_f32_e32 v47, v47, v49
	ds_bpermute_b32 v48, v154, v47
	s_waitcnt lgkmcnt(0)
	v_add_f32_e32 v47, v47, v48

; __device__ __forceinline__ void swa_unit(const SwaArgs& A, int b, int kv, int qblk, LAS unsigned char* lds, int wave) {
;     ...
;     __syncthreads();
;     for (int i = tid; i < 4 * LUTC_N; i += 512) lut[i] = A.lut[(kv * 4) * LUTC_N + i];
;     const int NT = 1 + (qblk < 2 ? qblk : 2);
;     for (int i = 0; i < NT; ++i) stage_tile<64>(lds + L_BUF + i * 16384, Kh + (size_t)(q0 - 64 * i) * 128, Vh + (size_t)(q0 - 64 * i) * 128, 128, 128, wid, lane);
.LBB0_761:
	s_mov_b32 s4, s93
	s_lshr_b32 s8, s88, 6
	v_mbcnt_lo_u32_b32 v0, -1, s4
	v_mbcnt_hi_u32_b32 v0, -1, v0
	v_add_u32_e32 v116, s94, v0
	s_movk_i32 s4, 0x800
	s_waitcnt vmcnt(0) lgkmcnt(0)
	v_readfirstlane_b32 s12, v116
	v_cmp_gt_i32_e32 vcc, s4, v116
	s_barrier
	s_and_saveexec_b64 s[4:5], vcc
	s_mov_b64 s[10:11], 0x800
	s_cbranch_execz .LBB0_764
	s_and_b32 s6, s8, 1
	v_lshl_add_u32 v0, s6, 11, v116
	v_readlane_b32 s7, v254, 13
	v_ashrrev_i32_e32 v1, 31, v0
	v_lshl_add_u32 v210, v116, 2, s7
	v_lshl_add_u64 v[0:1], v[0:1], 2, s[2:3]
	flat_load_dword v206, v[0:1]
	flat_load_dword v207, v[0:1] offset:2048
	v_add_co_u32_e32 v0, vcc, 0x1000, v0
	s_nop 1
	v_addc_co_u32_e32 v1, vcc, 0, v1, vcc
	flat_load_dword v208, v[0:1]
	flat_load_dword v209, v[0:1] offset:2048

; #define LAS __attribute__((address_space(3)))
; __device__ __forceinline__ void swa_unit(const SwaArgs& A, int b, int kv, int qblk, LAS unsigned char* lds, int wave) {
;     ...
;     for (int i = 0; i < NT; ++i) stage_tile<64>(lds + L_BUF + i * 16384, Kh + (size_t)(q0 - 64 * i) * 128, Vh + (size_t)(q0 - 64 * i) * 128, 128, 128, wid, lane);
;     const int qpos = q0 + 32 * (wid & 1) + r32;
;     bf16x8 qr[4];
;     { const bf16_t* qp = A.Q + (rowb + qpos) * 512 + qh * HD + hi * 8;
; #pragma unroll
;       for (int d0 = 0; d0 < 4; ++d0) qr[d0] = *(const bf16x8*)(qp + d0 * 16); }
;     float mref = 0.f, l = 0.f; f32x16 o[2], cn;
;     float zf = 0.f; asm volatile("" : "+v"(zf));
; #pragma unroll
;     for (int r = 0; r < 16; ++r) { o[0][r] = zf; o[1][r] = zf; cn[r] = zf; }
;     const LAS float* lg = lut + g * LUTC_N;
;     asm volatile("s_waitcnt vmcnt(0) lgkmcnt(0)" ::: "memory");
;     __syncthreads();
;     for (int i = 0; i < NT; ++i) {
;         const int kt0 = q0 - 64 * i;
;         const LAS unsigned char* slot = lds + L_BUF + i * 16384;
;         f32x16 p0, p1; qkt<64>(p0, p1, cn, slot, qr, r32, hi);
;         const int d0 = qpos - kt0 - 4 * hi;
;         const LAS float* lp = lg + (LUTC_TOP - d0);
; #pragma unroll
;         for (int r = 0; r < 16; ++r) { const int c = (r & 3) + 8 * (r >> 2);
;             const int dd0 = d0 - c, dd1 = d0 - c - 32;
;             p0[r] = (dd0 >= 0 && dd0 < CW) ? p0[r] + lp[c] : NEG; p1[r] = (dd1 >= 0 && dd1 < CW) ? p1[r] + lp[c + 32] : NEG; }
.LBB0_765:
	s_lshl_b64 s[22:23], s[92:93], 1
	v_lshl_add_u64 v[4:5], v[0:1], 0, s[22:23]
	s_mov_b32 m0, s8
	s_add_i32 s7, s7, -1
	global_load_lds_dwordx4 v[4:5], off
	v_lshl_add_u64 v[4:5], v[2:3], 0, s[22:23]
	s_add_i32 m0, s8, 0x2000
	s_addk_i32 s92, 0xe000
	global_load_lds_dwordx4 v[4:5], off
	s_addk_i32 s8, 0x4000
	s_cmp_eq_u32 s7, 0
	s_cbranch_scc0 .LBB0_765
	s_ashr_i32 s25, s12, 7
	s_lshl_b32 s6, s6, 2
	s_and_b32 s24, s88, 63
	s_add_i32 s10, s25, s6
	s_lshl_b64 s[6:7], s[4:5], 12
	s_lshl_b32 s4, s21, 5
	s_lshl_b32 s23, s24, 6
	s_and_b32 s13, s4, 32
	v_and_b32_e32 v118, 31, v116
	s_or_b32 s22, s13, s23
	v_or_b32_e32 v4, s22, v118
	v_or_b32_e32 v0, s6, v4
	v_mov_b32_e32 v1, s7
	v_lshlrev_b64 v[0:1], 10, v[0:1]
	s_lshl_b32 s8, s10, 6
	v_lshrrev_b32_e32 v119, 5, v117
	v_lshl_add_u64 v[0:1], s[0:1], 0, v[0:1]
	s_ashr_i32 s9, s8, 31
	v_lshl_add_u64 v[0:1], s[8:9], 1, v[0:1]
	v_lshlrev_b32_e32 v112, 4, v119
	v_lshl_add_u64 v[0:1], v[0:1], 0, v[112:113]
	flat_load_dwordx4 v[96:99], v[0:1]
	flat_load_dwordx4 v[100:103], v[0:1] offset:32
	flat_load_dwordx4 v[104:107], v[0:1] offset:64
	flat_load_dwordx4 v[108:111], v[0:1] offset:96
	v_lshlrev_b32_e32 v63, 10, v119
	v_lshlrev_b32_e32 v64, 4, v118
	v_mov_b32_e32 v32, 0
	v_add3_u32 v5, 0, v63, v64
	s_waitcnt vmcnt(0) lgkmcnt(0)
	s_waitcnt vmcnt(0) lgkmcnt(0)
	ds_write_b32 v210, v206
	ds_write_b32 v210, v207 offset:2048
	ds_write_b32 v210, v208 offset:4096
	ds_write_b32 v210, v209 offset:6144
	s_waitcnt lgkmcnt(0)
	s_barrier
	ds_read_b128 v[0:3], v5
	ds_read_b128 v[48:51], v5 offset:512
	ds_read_b128 v[52:55], v5 offset:2048
	ds_read_b128 v[56:59], v5 offset:2560
	ds_read_b128 v[66:69], v5 offset:4096
	ds_read_b128 v[70:73], v5 offset:4608
	ds_read_b128 v[74:77], v5 offset:6144
	ds_read_b128 v[78:81], v5 offset:6656
	s_lshl_b32 s25, s25, 11
	v_mov_b32_e32 v33, v32
	v_mov_b32_e32 v34, v32
	v_mov_b32_e32 v35, v32
	v_mov_b32_e32 v36, v32
	v_mov_b32_e32 v37, v32
	v_mov_b32_e32 v38, v32
	v_mov_b32_e32 v39, v32
	v_mov_b32_e32 v40, v32
	v_mov_b32_e32 v41, v32
	v_mov_b32_e32 v42, v32
	v_mov_b32_e32 v43, v32
	v_mov_b32_e32 v44, v32
	v_mov_b32_e32 v45, v32
	v_mov_b32_e32 v46, v32
	v_mov_b32_e32 v47, v32
	s_add_i32 s4, s25, 0
	v_lshlrev_b32_e32 v65, 2, v119
	v_sub_u32_e32 v60, v4, v65
	s_waitcnt lgkmcnt(7)
	v_mfma_f32_32x32x16_bf16 v[16:31], v[0:3], v[96:99], v[32:47]
	s_waitcnt lgkmcnt(6)
	v_mfma_f32_32x32x16_bf16 v[0:15], v[48:51], v[96:99], v[32:47]
	v_subrev_u32_e32 v51, s23, v60
	v_lshlrev_b32_e32 v48, 2, v51
	v_sub_u32_e32 v48, s4, v48
	v_add_u32_e32 v50, 0x11000, v48
	v_cmp_gt_u32_e32 vcc, s85, v51
	v_mov_b32_e32 v49, 0xf149f2ca
	v_mov_b32_e32 v48, 0xf149f2ca
	s_waitcnt lgkmcnt(5)
	v_mfma_f32_32x32x16_bf16 v[16:31], v[52:55], v[100:103], v[16:31]
	s_waitcnt lgkmcnt(4)
	v_mfma_f32_32x32x16_bf16 v[0:15], v[56:59], v[100:103], v[0:15]
	s_waitcnt lgkmcnt(3)
	v_mfma_f32_32x32x16_bf16 v[16:31], v[66:69], v[104:107], v[16:31]
	s_waitcnt lgkmcnt(2)
	v_mfma_f32_32x32x16_bf16 v[0:15], v[70:73], v[104:107], v[0:15]
	s_waitcnt lgkmcnt(1)
	v_mfma_f32_32x32x16_bf16 v[16:31], v[74:77], v[108:111], v[16:31]
	s_waitcnt lgkmcnt(0)
	v_mfma_f32_32x32x16_bf16 v[0:15], v[78:81], v[108:111], v[0:15]
	s_and_saveexec_b64 s[4:5], vcc
	s_cbranch_execz .LBB0_768
	ds_read_b32 v48, v50 offset:1020
	s_waitcnt lgkmcnt(0)
	s_nop 5
	v_add_f32_e32 v48, v16, v48
